# P8 epilogue: the 256 packed f32 ops (v_pk_fma/mul/add_f32) split into scalar f32 pairs (instruction selection in a VALU-bound epilogue)
# baseline (speedup 1.0000x reference)
; __device__ __forceinline__ unsigned pk4_fp8(float a, float b, float c, float d) { int w = __builtin_amdgcn_cvt_pk_fp8_f32(a, b, 0, false); w = __builtin_amdgcn_cvt_pk_fp8_f32(c, d, w, true); return (unsigned)w; }
;     static __device__ __forceinline__ f32x2 act2(f32x2 g, f32x2 u) {
;         g.x = __builtin_amdgcn_fmed3f(g.x, -24.0f, 7.0f); g.y = __builtin_amdgcn_fmed3f(g.y, -24.0f, 7.0f);
;         u.x = __builtin_amdgcn_fmed3f(u.x, -7.0f, 7.0f); u.y = __builtin_amdgcn_fmed3f(u.y, -7.0f, 7.0f);
;         f32x2 z = g * (-1.702f * 1.4426950408889634f);
;         f32x2 d; d.x = __builtin_amdgcn_exp2f(z.x); d.y = __builtin_amdgcn_exp2f(z.y);
;         d = d + 1.0f;
;         const float r = __builtin_amdgcn_rcpf(d.x * d.y);
;         f32x2 sg; sg.x = r * d.y; sg.y = r * d.x;
;         return (u + 1.0f) * (g * sg);
;     }
;     __device__ __forceinline__ void operator()(const f32x4 (&acc)[2][2][4][2], const pg8::Unit& u, int wr, int wc, int fr, int fq) const {
;         const int e = u.aux;
;         unsigned char* Ht = ws + WS_H2 + (size_t)u.pm * TSF8;
;         const int hc = u.pn * 128 + wc * 32 + 8 * fq;
;         const f32x4 bg0 = *(const f32x4*)(bgate + e * FF + hc), bg1 = *(const f32x4*)(bgate + e * FF + hc + 4);
;         const f32x4 bu0 = *(const f32x4*)(bup + e * FF + hc), bu1 = *(const f32x4*)(bup + e * FF + hc + 4);
; #pragma unroll
;         for (int ai = 0; ai < 2; ++ai)
; #pragma unroll
;             for (int m = 0; m < 4; ++m) { const int rl = ai * 128 + wr * 64 + m * 16 + fr;
;                 const f32x4 g0 = acc[ai][0][m][0] * (1.0f / 64.0f) + bg0, g1 = acc[ai][0][m][1] * (1.0f / 64.0f) + bg1, u0 = acc[ai][1][m][0] * (1.0f / 64.0f) + bu0, u1 = acc[ai][1][m][1] * (1.0f / 64.0f) + bu1;
;                 const f32x2 h0 = act2((f32x2){g0[0], g0[1]}, (f32x2){u0[0], u0[1]}), h1 = act2((f32x2){g0[2], g0[3]}, (f32x2){u0[2], u0[3]});
;                 const f32x2 h2 = act2((f32x2){g1[0], g1[1]}, (f32x2){u1[0], u1[1]}), h3 = act2((f32x2){g1[2], g1[3]}, (f32x2){u1[2], u1[3]});
;                 *(u32x2*)(Ht + (size_t)rl * FF + hc) = (u32x2){pk4_fp8(h0.x, h0.y, h1.x, h1.y), pk4_fp8(h2.x, h2.y, h3.x, h3.y)}; }
.Lmy_nobar0:
	s_ashr_i32 s23, s22, 31
	s_lshl_b64 s[22:23], s[22:23], 18
	v_mov_b32_e32 v24, v0
	s_add_u32 s22, s46, s22
	s_addc_u32 s23, s47, s23
	s_lshl_b32 s24, s62, 7
	v_lshrrev_b32_e32 v6, 1, v24
	v_and_or_b32 v6, v6, 24, s24
	s_lshl_b32 s24, s61, 10
	s_ashr_i32 s25, s24, 31
	v_or_b32_e32 v22, s45, v6
	s_lshl_b64 s[24:25], s[24:25], 2
	s_add_u32 s26, s84, s24
	v_ashrrev_i32_e32 v23, 31, v22
	s_addc_u32 s27, s85, s25
	v_lshlrev_b64 v[6:7], 2, v[22:23]
	v_lshl_add_u64 v[8:9], s[26:27], 0, v[6:7]
	s_add_u32 s24, s88, s24
	s_addc_u32 s25, s89, s25
	v_lshl_add_u64 v[6:7], s[24:25], 0, v[6:7]
	s_nop 0
	v_and_or_b32 v26, v24, 15, s44
	v_ashrrev_i32_e32 v27, 31, v26
	v_lshlrev_b64 v[32:33], 10, v[26:27]
	v_lshl_add_u64 v[24:25], s[22:23], 0, v[22:23]
	v_lshl_add_u64 v[22:23], v[24:25], 0, v[32:33]
	v_mov_b32_e32 v28, v198
	v_mov_b32_e32 v29, v198
	v_or_b32_e32 v30, 16, v26
	v_fma_f32 v34, v186, s16, v222
	v_fma_f32 v35, v187, s16, v223
	s_nop 0
	v_med3_f32 v34, v34, s48, v208
	v_med3_f32 v35, v35, s48, v208
	v_mul_f32_e32 v56, s18, v34
	v_mul_f32_e32 v57, s18, v35
	v_fma_f32 v32, v188, s16, v224
	v_fma_f32 v33, v189, s16, v225
	v_exp_f32_e32 v56, v56
	v_exp_f32_e32 v57, v57
	v_fma_f32 v38, v194, s16, v218
	v_fma_f32 v39, v195, s16, v219
	v_med3_f32 v32, v32, s48, v208
	v_med3_f32 v33, v33, s48, v208
	v_med3_f32 v38, v38, s48, v208
	v_med3_f32 v39, v39, s48, v208
	v_mul_f32_e32 v58, s18, v32
	v_mul_f32_e32 v59, s18, v33
	v_mul_f32_e32 v60, s18, v38
	v_mul_f32_e32 v61, s18, v39
	v_exp_f32_e32 v58, v58
	v_exp_f32_e32 v59, v59
	v_exp_f32_e32 v60, v60
	v_exp_f32_e32 v61, v61
	v_add_f32_e32 v56, 1.0, v56
	v_add_f32_e32 v57, 1.0, v57
	v_fma_f32 v36, v196, s16, v220
	v_fma_f32 v37, v197, s16, v221
	v_mul_f32_e32 v27, v56, v57
	v_med3_f32 v36, v36, s48, v208
	v_med3_f32 v37, v37, s48, v208
	v_fma_f32 v64, v172, s16, v228
	v_fma_f32 v65, v173, s16, v229
	v_rcp_f32_e32 v172, v27
	v_mul_f32_e32 v62, s18, v36
	v_mul_f32_e32 v63, s18, v37
	v_add_f32_e32 v58, 1.0, v58
	v_add_f32_e32 v59, 1.0, v59
	v_exp_f32_e32 v62, v62
	v_exp_f32_e32 v63, v63
	v_add_f32_e32 v60, 1.0, v60
	v_add_f32_e32 v61, 1.0, v61
	v_fma_f32 v50, v174, s16, v226
	v_fma_f32 v51, v175, s16, v227
	v_mul_f32_e32 v31, v58, v59
	v_mul_f32_e32 v173, v60, v61
	v_med3_f32 v50, v50, s49, v208
	v_med3_f32 v51, v51, s49, v208
	v_rcp_f32_e32 v174, v31
	v_mul_f32_e32 v232, v57, v172
	v_mul_f32_e32 v57, v56, v172
	v_mov_b32_e32 v56, v232
	v_add_f32_e32 v50, 1.0, v50
	v_add_f32_e32 v51, 1.0, v51
	v_mul_f32_e32 v34, v34, v56
	v_mul_f32_e32 v35, v35, v57
	v_add_f32_e32 v62, 1.0, v62
	v_add_f32_e32 v63, 1.0, v63
	v_mul_f32_e32 v34, v50, v34
	v_mul_f32_e32 v35, v51, v35
	v_fma_f32 v48, v176, s16, v228
	v_fma_f32 v49, v177, s16, v229
	v_mul_f32_e32 v175, v62, v63
	v_cvt_pk_fp8_f32 v28, v34, v35
	v_med3_f32 v48, v48, s49, v208
	v_med3_f32 v49, v49, s49, v208
	v_mul_f32_e32 v232, v59, v174
	v_mul_f32_e32 v59, v58, v174
	v_mov_b32_e32 v58, v232
	v_fma_f32 v42, v190, s16, v222
	v_fma_f32 v43, v191, s16, v223
	v_add_f32_e32 v48, 1.0, v48
	v_add_f32_e32 v49, 1.0, v49
	v_rcp_f32_e32 v176, v173
	v_mul_f32_e32 v32, v32, v58
	v_mul_f32_e32 v33, v33, v59
	v_med3_f32 v42, v42, s48, v208
	v_med3_f32 v43, v43, s48, v208
	v_mul_f32_e32 v32, v48, v32
	v_mul_f32_e32 v33, v49, v33
	v_fma_f32 v54, v178, s16, v214
	v_fma_f32 v55, v179, s16, v215
	v_cvt_pk_fp8_f32 v28, v32, v33 op_sel:[0,0,1]
	v_mul_f32_e32 v32, s18, v42
	v_mul_f32_e32 v33, s18, v43
	v_rcp_f32_e32 v178, v175
	v_exp_f32_e32 v32, v32
	v_exp_f32_e32 v33, v33
	v_med3_f32 v54, v54, s49, v208
	v_med3_f32 v55, v55, s49, v208
	v_mul_f32_e32 v232, v61, v176
	v_mul_f32_e32 v61, v60, v176
	v_mov_b32_e32 v60, v232
	v_add_f32_e32 v54, 1.0, v54
	v_add_f32_e32 v55, 1.0, v55
	v_mul_f32_e32 v38, v38, v60
	v_mul_f32_e32 v39, v39, v61
	v_fma_f32 v40, v192, s16, v224
	v_fma_f32 v41, v193, s16, v225
	v_fma_f32 v52, v180, s16, v216
	v_fma_f32 v53, v181, s16, v217
	v_mul_f32_e32 v38, v54, v38
	v_mul_f32_e32 v39, v55, v39
	v_med3_f32 v52, v52, s49, v208
	v_med3_f32 v53, v53, s49, v208
	v_mul_f32_e32 v232, v63, v178
	v_mul_f32_e32 v63, v62, v178
	v_mov_b32_e32 v62, v232
	v_cvt_pk_fp8_f32 v29, v38, v39
	v_add_f32_e32 v32, 1.0, v32
	v_add_f32_e32 v33, 1.0, v33
	v_med3_f32 v38, v40, s48, v208
	v_med3_f32 v39, v41, s48, v208
	v_add_f32_e32 v52, 1.0, v52
	v_add_f32_e32 v53, 1.0, v53
	v_mul_f32_e32 v36, v36, v62
	v_mul_f32_e32 v37, v37, v63
	v_mul_f32_e32 v27, v32, v33
	v_mul_f32_e32 v40, s18, v38
	v_mul_f32_e32 v41, s18, v39
	v_mul_f32_e32 v34, v52, v36
	v_mul_f32_e32 v35, v53, v37
	v_rcp_f32_e32 v36, v27
	v_exp_f32_e32 v40, v40
	v_exp_f32_e32 v41, v41
	v_fma_f32 v46, v182, s16, v218
	v_fma_f32 v47, v183, s16, v219
	v_mul_f32_e32 v232, v33, v36
	v_mul_f32_e32 v33, v32, v36
	v_mov_b32_e32 v32, v232
	v_fma_f32 v170, v170, s16, v226
	v_fma_f32 v171, v171, s16, v227
	v_add_f32_e32 v36, 1.0, v40
	v_add_f32_e32 v37, 1.0, v41
	v_cvt_pk_fp8_f32 v29, v34, v35 op_sel:[0,0,1]
	v_mul_f32_e32 v27, v36, v37
	v_rcp_f32_e32 v40, v27
	v_med3_f32 v34, v170, s49, v208
	v_med3_f32 v35, v171, s49, v208
	v_add_f32_e32 v34, 1.0, v34
	v_add_f32_e32 v35, 1.0, v35
	v_mul_f32_e32 v232, v37, v40
	v_mul_f32_e32 v37, v36, v40
	v_mov_b32_e32 v36, v232
	v_mul_f32_e32 v36, v38, v36
	v_mul_f32_e32 v37, v39, v37
	v_med3_f32 v38, v46, s48, v208
	v_med3_f32 v39, v47, s48, v208
	v_mul_f32_e32 v40, s18, v38
	v_mul_f32_e32 v41, s18, v39
	v_mul_f32_e32 v32, v42, v32
	v_mul_f32_e32 v33, v43, v33
	v_exp_f32_e32 v40, v40
	v_exp_f32_e32 v41, v41
	v_mul_f32_e32 v32, v34, v32
	v_mul_f32_e32 v33, v35, v33
	v_med3_f32 v34, v64, s49, v208
	v_med3_f32 v35, v65, s49, v208
	v_add_f32_e32 v34, 1.0, v34
	v_add_f32_e32 v35, 1.0, v35
; __device__ __forceinline__ unsigned pk4_fp8(float a, float b, float c, float d) { int w = __builtin_amdgcn_cvt_pk_fp8_f32(a, b, 0, false); w = __builtin_amdgcn_cvt_pk_fp8_f32(c, d, w, true); return (unsigned)w; }
;     __device__ __forceinline__ void operator()(const f32x4 (&acc)[2][2][4][2], const pg8::Unit& u, int wr, int wc, int fr, int fq) const {
;     ...
;             for (int m = 0; m < 4; ++m) { const int rl = ai * 128 + wr * 64 + m * 16 + fr;
;                 const f32x4 g0 = acc[ai][0][m][0] * (1.0f / 64.0f) + bg0, g1 = acc[ai][0][m][1] * (1.0f / 64.0f) + bg1, u0 = acc[ai][1][m][0] * (1.0f / 64.0f) + bu0, u1 = acc[ai][1][m][1] * (1.0f / 64.0f) + bu1;
;                 const f32x2 h0 = act2((f32x2){g0[0], g0[1]}, (f32x2){u0[0], u0[1]}), h1 = act2((f32x2){g0[2], g0[3]}, (f32x2){u0[2], u0[3]});
;                 const f32x2 h2 = act2((f32x2){g1[0], g1[1]}, (f32x2){u1[0], u1[1]}), h3 = act2((f32x2){g1[2], g1[3]}, (f32x2){u1[2], u1[3]});
;                 *(u32x2*)(Ht + (size_t)rl * FF + hc) = (u32x2){pk4_fp8(h0.x, h0.y, h1.x, h1.y), pk4_fp8(h2.x, h2.y, h3.x, h3.y)}; }
	v_fma_f32 v44, v184, s16, v220
	v_fma_f32 v45, v185, s16, v221
	v_mul_f32_e32 v34, v34, v36
	v_mul_f32_e32 v35, v35, v37
	v_add_f32_e32 v36, 1.0, v40
	v_add_f32_e32 v37, 1.0, v41
	v_med3_f32 v42, v44, s48, v208
	v_mul_f32_e32 v27, v36, v37
	v_med3_f32 v43, v45, s48, v208
	v_rcp_f32_e32 v40, v27
	v_mul_f32_e32 v44, s18, v42
	v_mul_f32_e32 v45, s18, v43
	global_store_dwordx2 v[22:23], v[28:29], off
	v_exp_f32_e32 v44, v44
	v_exp_f32_e32 v45, v45
	v_mul_f32_e32 v232, v37, v40
	v_mul_f32_e32 v37, v36, v40
	v_mov_b32_e32 v36, v232
	v_mul_f32_e32 v36, v38, v36
	v_mul_f32_e32 v37, v39, v37
	v_fma_f32 v28, v166, s16, v214
	v_fma_f32 v29, v167, s16, v215
	v_add_f32_e32 v38, 1.0, v44
	v_add_f32_e32 v39, 1.0, v45
	v_med3_f32 v28, v28, s49, v208
	v_mul_f32_e32 v27, v38, v39
	v_rcp_f32_e32 v40, v27
	v_med3_f32 v29, v29, s49, v208
	v_add_f32_e32 v28, 1.0, v28
	v_add_f32_e32 v29, 1.0, v29
	v_fma_f32 v168, v168, s16, v216
	v_fma_f32 v169, v169, s16, v217
	v_mul_f32_e32 v232, v39, v40
	v_mul_f32_e32 v39, v38, v40
	v_mov_b32_e32 v38, v232
	v_mov_b32_e32 v40, v198
	v_cvt_pk_fp8_f32 v40, v32, v33
	v_fma_f32 v32, v154, s16, v222
	v_fma_f32 v33, v155, s16, v223
	v_mul_f32_e32 v28, v28, v36
	v_mul_f32_e32 v29, v29, v37
	v_med3_f32 v32, v32, s48, v208
	v_med3_f32 v33, v33, s48, v208
	v_mov_b32_e32 v41, v198
	v_mul_f32_e32 v44, s18, v32
	v_mul_f32_e32 v45, s18, v33
	v_cvt_pk_fp8_f32 v41, v28, v29
	v_exp_f32_e32 v44, v44
	v_exp_f32_e32 v45, v45
	v_med3_f32 v36, v168, s49, v208
	v_med3_f32 v37, v169, s49, v208
	v_add_f32_e32 v36, 1.0, v36
	v_add_f32_e32 v37, 1.0, v37
	v_mul_f32_e32 v28, v42, v38
	v_mul_f32_e32 v29, v43, v39
	v_ashrrev_i32_e32 v31, 31, v30
	v_mul_f32_e32 v28, v36, v28
	v_mul_f32_e32 v29, v37, v29
	v_add_f32_e32 v44, 1.0, v44
	v_add_f32_e32 v45, 1.0, v45
	v_cvt_pk_fp8_f32 v41, v28, v29 op_sel:[0,0,1]
	v_lshlrev_b64 v[28:29], 10, v[30:31]
	v_fma_f32 v30, v156, s16, v224
	v_fma_f32 v31, v157, s16, v225
	v_mul_f32_e32 v27, v44, v45
	v_med3_f32 v30, v30, s48, v208
	v_med3_f32 v31, v31, s48, v208
	v_rcp_f32_e32 v48, v27
	v_mul_f32_e32 v50, s18, v30
	v_mul_f32_e32 v51, s18, v31
	v_cvt_pk_fp8_f32 v40, v34, v35 op_sel:[0,0,1]
	v_exp_f32_e32 v50, v50
	v_exp_f32_e32 v51, v51
	v_mul_f32_e32 v232, v45, v48
	v_mul_f32_e32 v45, v44, v48
	v_mov_b32_e32 v44, v232
	v_mul_f32_e32 v32, v32, v44
	v_mul_f32_e32 v33, v33, v45
	v_lshl_add_u64 v[28:29], v[24:25], 0, v[28:29]
	v_add_f32_e32 v44, 1.0, v50
	v_add_f32_e32 v45, 1.0, v51
	global_store_dwordx2 v[28:29], v[40:41], off
	v_mul_f32_e32 v27, v44, v45
	v_rcp_f32_e32 v48, v27
	v_fma_f32 v40, v162, s16, v226
	v_fma_f32 v41, v163, s16, v227
	v_fma_f32 v36, v150, s16, v218
	v_fma_f32 v37, v151, s16, v219
	v_med3_f32 v40, v40, s49, v208
	v_med3_f32 v41, v41, s49, v208
	v_add_f32_e32 v40, 1.0, v40
	v_add_f32_e32 v41, 1.0, v41
	v_med3_f32 v36, v36, s48, v208
	v_mul_f32_e32 v32, v40, v32
	v_mul_f32_e32 v33, v41, v33
	v_mul_f32_e32 v40, v45, v48
	v_mul_f32_e32 v41, v44, v48
	v_med3_f32 v37, v37, s48, v208
	v_mul_f32_e32 v30, v30, v40
	v_mul_f32_e32 v31, v31, v41
	v_mul_f32_e32 v40, s18, v36
	v_mul_f32_e32 v41, s18, v37
	v_fma_f32 v38, v164, s16, v228
	v_fma_f32 v39, v165, s16, v229
	v_exp_f32_e32 v40, v40
	v_exp_f32_e32 v41, v41
	v_fma_f32 v34, v152, s16, v220
	v_fma_f32 v35, v153, s16, v221
	v_med3_f32 v38, v38, s49, v208
	v_med3_f32 v39, v39, s49, v208
	v_add_f32_e32 v40, 1.0, v40
	v_add_f32_e32 v41, 1.0, v41
	v_fma_f32 v46, v158, s16, v214
	v_fma_f32 v47, v159, s16, v215
	v_add_f32_e32 v38, 1.0, v38
	v_add_f32_e32 v39, 1.0, v39
	v_mul_f32_e32 v27, v40, v41
	v_med3_f32 v34, v34, s48, v208
	v_med3_f32 v35, v35, s48, v208
	v_mul_f32_e32 v30, v38, v30
	v_mul_f32_e32 v31, v39, v31
	v_med3_f32 v38, v46, s49, v208
	v_med3_f32 v39, v47, s49, v208
	v_rcp_f32_e32 v44, v27
	v_mul_f32_e32 v46, s18, v34
	v_mul_f32_e32 v47, s18, v35
	v_fma_f32 v42, v160, s16, v216
	v_fma_f32 v43, v161, s16, v217
	v_exp_f32_e32 v46, v46
	v_exp_f32_e32 v47, v47
	v_mul_f32_e32 v232, v41, v44
	v_mul_f32_e32 v41, v40, v44
	v_mov_b32_e32 v40, v232
	v_mul_f32_e32 v36, v36, v40
	v_mul_f32_e32 v37, v37, v41
	v_add_f32_e32 v38, 1.0, v38
	v_add_f32_e32 v39, 1.0, v39
	v_add_f32_e32 v40, 1.0, v46
	v_add_f32_e32 v41, 1.0, v47
	v_mul_f32_e32 v36, v38, v36
	v_mul_f32_e32 v37, v39, v37
	v_mul_f32_e32 v27, v40, v41
	v_rcp_f32_e32 v44, v27
	v_med3_f32 v38, v42, s49, v208
	v_med3_f32 v39, v43, s49, v208
	v_mov_b32_e32 v42, v198
	v_mov_b32_e32 v43, v198
	v_cvt_pk_fp8_f32 v42, v32, v33
	v_cvt_pk_fp8_f32 v43, v36, v37
	v_mul_f32_e32 v232, v41, v44
	v_mul_f32_e32 v41, v40, v44
	v_mov_b32_e32 v40, v232
	v_add_f32_e32 v38, 1.0, v38
	v_add_f32_e32 v39, 1.0, v39
	v_mul_f32_e32 v32, v34, v40
	v_mul_f32_e32 v33, v35, v41
	v_or_b32_e32 v28, 32, v26
	v_mul_f32_e32 v32, v38, v32
	v_mul_f32_e32 v33, v39, v33
	v_cvt_pk_fp8_f32 v42, v30, v31 op_sel:[0,0,1]
	v_cvt_pk_fp8_f32 v43, v32, v33 op_sel:[0,0,1]
	v_ashrrev_i32_e32 v29, 31, v28
	v_lshlrev_b64 v[28:29], 10, v[28:29]
	v_fma_f32 v30, v138, s16, v222
	v_fma_f32 v31, v139, s16, v223
	v_lshl_add_u64 v[28:29], v[24:25], 0, v[28:29]
	v_med3_f32 v30, v30, s48, v208
	v_med3_f32 v31, v31, s48, v208
	global_store_dwordx2 v[28:29], v[42:43], off
	v_mul_f32_e32 v42, s18, v30
	v_mul_f32_e32 v43, s18, v31
	v_fma_f32 v28, v140, s16, v224
	v_fma_f32 v29, v141, s16, v225
	v_exp_f32_e32 v42, v42
	v_exp_f32_e32 v43, v43
	v_med3_f32 v28, v28, s48, v208
	v_med3_f32 v29, v29, s48, v208
	v_mul_f32_e32 v48, s18, v28
	v_mul_f32_e32 v49, s18, v29
	v_add_f32_e32 v42, 1.0, v42
	v_add_f32_e32 v43, 1.0, v43
	v_exp_f32_e32 v48, v48
	v_mul_f32_e32 v27, v42, v43
	v_rcp_f32_e32 v46, v27
	v_exp_f32_e32 v49, v49
	v_fma_f32 v38, v146, s16, v226
	v_fma_f32 v39, v147, s16, v227
; __device__ __forceinline__ unsigned pk4_fp8(float a, float b, float c, float d) { int w = __builtin_amdgcn_cvt_pk_fp8_f32(a, b, 0, false); w = __builtin_amdgcn_cvt_pk_fp8_f32(c, d, w, true); return (unsigned)w; }
;     __device__ __forceinline__ void operator()(const f32x4 (&acc)[2][2][4][2], const pg8::Unit& u, int wr, int wc, int fr, int fq) const {
;     ...
;             for (int m = 0; m < 4; ++m) { const int rl = ai * 128 + wr * 64 + m * 16 + fr;
;                 const f32x4 g0 = acc[ai][0][m][0] * (1.0f / 64.0f) + bg0, g1 = acc[ai][0][m][1] * (1.0f / 64.0f) + bg1, u0 = acc[ai][1][m][0] * (1.0f / 64.0f) + bu0, u1 = acc[ai][1][m][1] * (1.0f / 64.0f) + bu1;
;                 const f32x2 h0 = act2((f32x2){g0[0], g0[1]}, (f32x2){u0[0], u0[1]}), h1 = act2((f32x2){g0[2], g0[3]}, (f32x2){u0[2], u0[3]});
;                 const f32x2 h2 = act2((f32x2){g1[0], g1[1]}, (f32x2){u1[0], u1[1]}), h3 = act2((f32x2){g1[2], g1[3]}, (f32x2){u1[2], u1[3]});
;                 *(u32x2*)(Ht + (size_t)rl * FF + hc) = (u32x2){pk4_fp8(h0.x, h0.y, h1.x, h1.y), pk4_fp8(h2.x, h2.y, h3.x, h3.y)}; }
	v_fma_f32 v34, v134, s16, v218
	v_fma_f32 v35, v135, s16, v219
	v_mul_f32_e32 v232, v43, v46
	v_mul_f32_e32 v43, v42, v46
	v_mov_b32_e32 v42, v232
	v_mul_f32_e32 v30, v30, v42
	v_mul_f32_e32 v31, v31, v43
	v_add_f32_e32 v42, 1.0, v48
	v_add_f32_e32 v43, 1.0, v49
	v_med3_f32 v38, v38, s49, v208
	v_mul_f32_e32 v27, v42, v43
	v_rcp_f32_e32 v46, v27
	v_med3_f32 v39, v39, s49, v208
	v_add_f32_e32 v38, 1.0, v38
	v_add_f32_e32 v39, 1.0, v39
	v_med3_f32 v34, v34, s48, v208
	v_mul_f32_e32 v30, v38, v30
	v_mul_f32_e32 v31, v39, v31
	v_mul_f32_e32 v38, v43, v46
	v_mul_f32_e32 v39, v42, v46
	v_med3_f32 v35, v35, s48, v208
	v_mul_f32_e32 v28, v28, v38
	v_mul_f32_e32 v29, v29, v39
	v_mul_f32_e32 v38, s18, v34
	v_mul_f32_e32 v39, s18, v35
	v_fma_f32 v36, v148, s16, v228
	v_fma_f32 v37, v149, s16, v229
	v_exp_f32_e32 v38, v38
	v_exp_f32_e32 v39, v39
	v_fma_f32 v32, v136, s16, v220
	v_fma_f32 v33, v137, s16, v221
	v_med3_f32 v36, v36, s49, v208
	v_med3_f32 v37, v37, s49, v208
	v_add_f32_e32 v38, 1.0, v38
	v_add_f32_e32 v39, 1.0, v39
	v_fma_f32 v44, v142, s16, v214
	v_fma_f32 v45, v143, s16, v215
	v_add_f32_e32 v36, 1.0, v36
	v_add_f32_e32 v37, 1.0, v37
	v_mul_f32_e32 v27, v38, v39
	v_med3_f32 v32, v32, s48, v208
	v_med3_f32 v33, v33, s48, v208
	v_mul_f32_e32 v28, v36, v28
	v_mul_f32_e32 v29, v37, v29
	v_med3_f32 v36, v44, s49, v208
	v_med3_f32 v37, v45, s49, v208
	v_rcp_f32_e32 v42, v27
	v_mul_f32_e32 v44, s18, v32
	v_mul_f32_e32 v45, s18, v33
	v_or_b32_e32 v26, 48, v26
	v_exp_f32_e32 v44, v44
	v_exp_f32_e32 v45, v45
	v_mul_f32_e32 v232, v39, v42
	v_mul_f32_e32 v39, v38, v42
	v_mov_b32_e32 v38, v232
	v_mul_f32_e32 v34, v34, v38
	v_mul_f32_e32 v35, v35, v39
	v_fma_f32 v40, v144, s16, v216
	v_fma_f32 v41, v145, s16, v217
	v_add_f32_e32 v38, 1.0, v44
	v_add_f32_e32 v39, 1.0, v45
	v_add_f32_e32 v36, 1.0, v36
	v_add_f32_e32 v37, 1.0, v37
	v_mul_f32_e32 v27, v38, v39
	v_rcp_f32_e32 v42, v27
	v_mul_f32_e32 v34, v36, v34
	v_mul_f32_e32 v35, v37, v35
	v_med3_f32 v36, v40, s49, v208
	v_med3_f32 v37, v41, s49, v208
	v_mov_b32_e32 v40, v198
	v_mov_b32_e32 v41, v198
	v_ashrrev_i32_e32 v27, 31, v26
	v_cvt_pk_fp8_f32 v40, v30, v31
	v_cvt_pk_fp8_f32 v41, v34, v35
	v_lshlrev_b64 v[26:27], 10, v[26:27]
	v_mul_f32_e32 v232, v39, v42
	v_mul_f32_e32 v39, v38, v42
	v_mov_b32_e32 v38, v232
	v_lshl_add_u64 v[24:25], v[24:25], 0, v[26:27]
	v_fma_f32 v26, v122, s16, v222
	v_fma_f32 v27, v123, s16, v223
	v_add_f32_e32 v36, 1.0, v36
	v_add_f32_e32 v37, 1.0, v37
	v_mul_f32_e32 v30, v32, v38
	v_mul_f32_e32 v31, v33, v39
	v_med3_f32 v26, v26, s48, v208
	v_med3_f32 v27, v27, s48, v208
	v_mul_f32_e32 v30, v36, v30
	v_mul_f32_e32 v31, v37, v31
	v_mul_f32_e32 v38, s18, v26
	v_mul_f32_e32 v39, s18, v27
	v_cvt_pk_fp8_f32 v40, v28, v29 op_sel:[0,0,1]
	v_cvt_pk_fp8_f32 v41, v30, v31 op_sel:[0,0,1]
	v_exp_f32_e32 v38, v38
	v_exp_f32_e32 v39, v39
	v_fma_f32 v34, v130, s16, v226
	v_fma_f32 v35, v131, s16, v227
	global_store_dwordx2 v[24:25], v[40:41], off
	v_fma_f32 v24, v124, s16, v224
	v_fma_f32 v25, v125, s16, v225
	v_add_f32_e32 v38, 1.0, v38
	v_add_f32_e32 v39, 1.0, v39
	v_med3_f32 v24, v24, s48, v208
	v_mul_f32_e32 v42, v38, v39
	v_med3_f32 v25, v25, s48, v208
	v_rcp_f32_e32 v42, v42
	v_mul_f32_e32 v44, s18, v24
	v_mul_f32_e32 v45, s18, v25
	v_med3_f32 v34, v34, s49, v208
	v_exp_f32_e32 v44, v44
	v_exp_f32_e32 v45, v45
	v_mul_f32_e32 v232, v39, v42
	v_mul_f32_e32 v39, v38, v42
	v_mov_b32_e32 v38, v232
	v_mul_f32_e32 v26, v26, v38
	v_mul_f32_e32 v27, v27, v39
	v_med3_f32 v35, v35, s49, v208
	v_add_f32_e32 v38, 1.0, v44
	v_add_f32_e32 v39, 1.0, v45
	v_fma_f32 v30, v118, s16, v218
	v_fma_f32 v31, v119, s16, v219
	v_mul_f32_e32 v42, v38, v39
	v_rcp_f32_e32 v42, v42
	v_add_f32_e32 v34, 1.0, v34
	v_add_f32_e32 v35, 1.0, v35
	v_med3_f32 v30, v30, s48, v208
	v_mul_f32_e32 v26, v34, v26
	v_mul_f32_e32 v27, v35, v27
	v_mul_f32_e32 v34, v39, v42
	v_mul_f32_e32 v35, v38, v42
	v_med3_f32 v31, v31, s48, v208
	v_mul_f32_e32 v24, v24, v34
	v_mul_f32_e32 v25, v25, v35
	v_mul_f32_e32 v34, s18, v30
	v_mul_f32_e32 v35, s18, v31
	v_fma_f32 v32, v132, s16, v228
	v_fma_f32 v33, v133, s16, v229
	v_exp_f32_e32 v34, v34
	v_exp_f32_e32 v35, v35
	v_fma_f32 v28, v120, s16, v220
	v_fma_f32 v29, v121, s16, v221
	v_med3_f32 v32, v32, s49, v208
	v_med3_f32 v33, v33, s49, v208
	v_add_f32_e32 v34, 1.0, v34
	v_add_f32_e32 v35, 1.0, v35
	v_fma_f32 v40, v126, s16, v214
	v_fma_f32 v41, v127, s16, v215
	v_add_f32_e32 v32, 1.0, v32
	v_add_f32_e32 v33, 1.0, v33
	v_mul_f32_e32 v38, v34, v35
	v_med3_f32 v28, v28, s48, v208
	v_med3_f32 v29, v29, s48, v208
	v_mul_f32_e32 v24, v32, v24
	v_mul_f32_e32 v25, v33, v25
	v_med3_f32 v32, v40, s49, v208
	v_med3_f32 v33, v41, s49, v208
	v_rcp_f32_e32 v38, v38
	v_mul_f32_e32 v40, s18, v28
	v_mul_f32_e32 v41, s18, v29
	v_fma_f32 v36, v128, s16, v216
	v_fma_f32 v37, v129, s16, v217
	v_exp_f32_e32 v40, v40
	v_exp_f32_e32 v41, v41
	v_mul_f32_e32 v232, v35, v38
	v_mul_f32_e32 v35, v34, v38
	v_mov_b32_e32 v34, v232
	v_mul_f32_e32 v30, v30, v34
	v_mul_f32_e32 v31, v31, v35
	v_add_f32_e32 v32, 1.0, v32
	v_add_f32_e32 v33, 1.0, v33
	v_add_f32_e32 v34, 1.0, v40
	v_add_f32_e32 v35, 1.0, v41
	v_mul_f32_e32 v30, v32, v30
	v_mul_f32_e32 v31, v33, v31
	v_mul_f32_e32 v38, v34, v35
	v_rcp_f32_e32 v38, v38
	v_med3_f32 v33, v37, s49, v208
	v_mov_b32_e32 v37, v198
	v_cvt_pk_fp8_f32 v37, v30, v31
	v_med3_f32 v32, v36, s49, v208
	v_mul_f32_e32 v232, v35, v38
	v_mul_f32_e32 v35, v34, v38
	v_mov_b32_e32 v34, v232
	v_mov_b32_e32 v36, v198
	v_add_f32_e32 v32, 1.0, v32
	v_add_f32_e32 v33, 1.0, v33
	v_cvt_pk_fp8_f32 v36, v26, v27
	v_mul_f32_e32 v26, v28, v34
	v_mul_f32_e32 v27, v29, v35
	v_fma_f32 v34, v114, s16, v226
; __device__ __forceinline__ unsigned pk4_fp8(float a, float b, float c, float d) { int w = __builtin_amdgcn_cvt_pk_fp8_f32(a, b, 0, false); w = __builtin_amdgcn_cvt_pk_fp8_f32(c, d, w, true); return (unsigned)w; }
;     __device__ __forceinline__ void operator()(const f32x4 (&acc)[2][2][4][2], const pg8::Unit& u, int wr, int wc, int fr, int fq) const {
;     ...
;             for (int m = 0; m < 4; ++m) { const int rl = ai * 128 + wr * 64 + m * 16 + fr;
;                 const f32x4 g0 = acc[ai][0][m][0] * (1.0f / 64.0f) + bg0, g1 = acc[ai][0][m][1] * (1.0f / 64.0f) + bg1, u0 = acc[ai][1][m][0] * (1.0f / 64.0f) + bu0, u1 = acc[ai][1][m][1] * (1.0f / 64.0f) + bu1;
;                 const f32x2 h0 = act2((f32x2){g0[0], g0[1]}, (f32x2){u0[0], u0[1]}), h1 = act2((f32x2){g0[2], g0[3]}, (f32x2){u0[2], u0[3]});
;                 const f32x2 h2 = act2((f32x2){g1[0], g1[1]}, (f32x2){u1[0], u1[1]}), h3 = act2((f32x2){g1[2], g1[3]}, (f32x2){u1[2], u1[3]});
;                 *(u32x2*)(Ht + (size_t)rl * FF + hc) = (u32x2){pk4_fp8(h0.x, h0.y, h1.x, h1.y), pk4_fp8(h2.x, h2.y, h3.x, h3.y)}; }
	v_fma_f32 v35, v115, s16, v227
	v_mul_f32_e32 v26, v32, v26
	v_mul_f32_e32 v27, v33, v27
	v_cvt_pk_fp8_f32 v36, v24, v25 op_sel:[0,0,1]
	v_cvt_pk_fp8_f32 v37, v26, v27 op_sel:[0,0,1]
	v_fma_f32 v26, v106, s16, v222
	v_fma_f32 v27, v107, s16, v223
	v_add_co_u32_e32 v24, vcc, s50, v22
	v_med3_f32 v26, v26, s48, v208
	v_med3_f32 v27, v27, s48, v208
	v_mul_f32_e32 v38, s18, v26
	v_mul_f32_e32 v39, s18, v27
	v_addc_co_u32_e32 v25, vcc, 0, v23, vcc
	v_exp_f32_e32 v38, v38
	v_exp_f32_e32 v39, v39
	global_store_dwordx2 v[24:25], v[36:37], off
	v_fma_f32 v24, v108, s16, v224
	v_fma_f32 v25, v109, s16, v225
	v_med3_f32 v34, v34, s49, v208
	v_add_f32_e32 v38, 1.0, v38
	v_add_f32_e32 v39, 1.0, v39
	v_med3_f32 v24, v24, s48, v208
	v_mul_f32_e32 v42, v38, v39
	v_med3_f32 v25, v25, s48, v208
	v_rcp_f32_e32 v42, v42
	v_mul_f32_e32 v44, s18, v24
	v_mul_f32_e32 v45, s18, v25
	v_med3_f32 v35, v35, s49, v208
	v_exp_f32_e32 v44, v44
	v_exp_f32_e32 v45, v45
	v_mul_f32_e32 v232, v39, v42
	v_mul_f32_e32 v39, v38, v42
	v_mov_b32_e32 v38, v232
	v_mul_f32_e32 v26, v26, v38
	v_mul_f32_e32 v27, v27, v39
	v_fma_f32 v30, v102, s16, v218
	v_fma_f32 v31, v103, s16, v219
	v_add_f32_e32 v38, 1.0, v44
	v_add_f32_e32 v39, 1.0, v45
	v_add_f32_e32 v34, 1.0, v34
	v_add_f32_e32 v35, 1.0, v35
	v_mul_f32_e32 v42, v38, v39
	v_rcp_f32_e32 v42, v42
	v_mul_f32_e32 v26, v34, v26
	v_mul_f32_e32 v27, v35, v27
	v_med3_f32 v30, v30, s48, v208
	v_med3_f32 v31, v31, s48, v208
	v_mul_f32_e32 v34, v39, v42
	v_mul_f32_e32 v35, v38, v42
	v_mul_f32_e32 v24, v24, v34
	v_mul_f32_e32 v25, v25, v35
	v_mul_f32_e32 v34, s18, v30
	v_mul_f32_e32 v35, s18, v31
	v_fma_f32 v32, v116, s16, v228
	v_fma_f32 v33, v117, s16, v229
	v_exp_f32_e32 v34, v34
	v_exp_f32_e32 v35, v35
	v_fma_f32 v28, v104, s16, v220
	v_fma_f32 v29, v105, s16, v221
	v_med3_f32 v32, v32, s49, v208
	v_med3_f32 v33, v33, s49, v208
	v_add_f32_e32 v34, 1.0, v34
	v_add_f32_e32 v35, 1.0, v35
	v_fma_f32 v40, v110, s16, v214
	v_fma_f32 v41, v111, s16, v215
	v_add_f32_e32 v32, 1.0, v32
	v_add_f32_e32 v33, 1.0, v33
	v_mul_f32_e32 v38, v34, v35
	v_med3_f32 v28, v28, s48, v208
	v_med3_f32 v29, v29, s48, v208
	v_mul_f32_e32 v24, v32, v24
	v_mul_f32_e32 v25, v33, v25
	v_med3_f32 v32, v40, s49, v208
	v_med3_f32 v33, v41, s49, v208
	v_rcp_f32_e32 v38, v38
	v_mul_f32_e32 v40, s18, v28
	v_mul_f32_e32 v41, s18, v29
	v_fma_f32 v36, v112, s16, v216
	v_fma_f32 v37, v113, s16, v217
	v_exp_f32_e32 v40, v40
	v_exp_f32_e32 v41, v41
	v_mul_f32_e32 v232, v35, v38
	v_mul_f32_e32 v35, v34, v38
	v_mov_b32_e32 v34, v232
	v_mul_f32_e32 v30, v30, v34
	v_mul_f32_e32 v31, v31, v35
	v_add_f32_e32 v32, 1.0, v32
	v_add_f32_e32 v33, 1.0, v33
	v_add_f32_e32 v34, 1.0, v40
	v_add_f32_e32 v35, 1.0, v41
	v_mul_f32_e32 v30, v32, v30
	v_mul_f32_e32 v31, v33, v31
	v_mul_f32_e32 v38, v34, v35
	v_rcp_f32_e32 v38, v38
	v_med3_f32 v33, v37, s49, v208
	v_mov_b32_e32 v37, v198
	v_cvt_pk_fp8_f32 v37, v30, v31
	v_med3_f32 v32, v36, s49, v208
	v_mul_f32_e32 v232, v35, v38
	v_mul_f32_e32 v35, v34, v38
	v_mov_b32_e32 v34, v232
	v_mov_b32_e32 v36, v198
	v_add_f32_e32 v32, 1.0, v32
	v_add_f32_e32 v33, 1.0, v33
	v_cvt_pk_fp8_f32 v36, v26, v27
	v_mul_f32_e32 v26, v28, v34
	v_mul_f32_e32 v27, v29, v35
	v_fma_f32 v34, v98, s16, v226
	v_fma_f32 v35, v99, s16, v227
	v_mul_f32_e32 v26, v32, v26
	v_mul_f32_e32 v27, v33, v27
	v_cvt_pk_fp8_f32 v36, v24, v25 op_sel:[0,0,1]
	v_cvt_pk_fp8_f32 v37, v26, v27 op_sel:[0,0,1]
	v_fma_f32 v26, v90, s16, v222
	v_fma_f32 v27, v91, s16, v223
	v_add_co_u32_e32 v24, vcc, s51, v22
	v_med3_f32 v26, v26, s48, v208
	v_med3_f32 v27, v27, s48, v208
	v_mul_f32_e32 v38, s18, v26
	v_mul_f32_e32 v39, s18, v27
	v_addc_co_u32_e32 v25, vcc, 0, v23, vcc
	v_exp_f32_e32 v38, v38
	v_exp_f32_e32 v39, v39
	global_store_dwordx2 v[24:25], v[36:37], off
	v_fma_f32 v24, v92, s16, v224
	v_fma_f32 v25, v93, s16, v225
	v_med3_f32 v34, v34, s49, v208
	v_add_f32_e32 v38, 1.0, v38
	v_add_f32_e32 v39, 1.0, v39
	v_med3_f32 v24, v24, s48, v208
	v_mul_f32_e32 v42, v38, v39
	v_med3_f32 v25, v25, s48, v208
	v_rcp_f32_e32 v42, v42
	v_mul_f32_e32 v44, s18, v24
	v_mul_f32_e32 v45, s18, v25
	v_med3_f32 v35, v35, s49, v208
	v_exp_f32_e32 v44, v44
	v_exp_f32_e32 v45, v45
	v_mul_f32_e32 v232, v39, v42
	v_mul_f32_e32 v39, v38, v42
	v_mov_b32_e32 v38, v232
	v_mul_f32_e32 v26, v26, v38
	v_mul_f32_e32 v27, v27, v39
	v_fma_f32 v30, v86, s16, v218
	v_fma_f32 v31, v87, s16, v219
	v_add_f32_e32 v38, 1.0, v44
	v_add_f32_e32 v39, 1.0, v45
	v_add_f32_e32 v34, 1.0, v34
	v_add_f32_e32 v35, 1.0, v35
	v_mul_f32_e32 v42, v38, v39
	v_rcp_f32_e32 v42, v42
	v_mul_f32_e32 v26, v34, v26
	v_mul_f32_e32 v27, v35, v27
	v_med3_f32 v30, v30, s48, v208
	v_med3_f32 v31, v31, s48, v208
	v_mul_f32_e32 v34, v39, v42
	v_mul_f32_e32 v35, v38, v42
	v_mul_f32_e32 v24, v24, v34
	v_mul_f32_e32 v25, v25, v35
	v_mul_f32_e32 v34, s18, v30
	v_mul_f32_e32 v35, s18, v31
	v_fma_f32 v32, v100, s16, v228
	v_fma_f32 v33, v101, s16, v229
	v_exp_f32_e32 v34, v34
	v_exp_f32_e32 v35, v35
	v_fma_f32 v28, v88, s16, v220
	v_fma_f32 v29, v89, s16, v221
	v_med3_f32 v32, v32, s49, v208
	v_med3_f32 v33, v33, s49, v208
	v_add_f32_e32 v34, 1.0, v34
; __device__ __forceinline__ unsigned pk4_fp8(float a, float b, float c, float d) { int w = __builtin_amdgcn_cvt_pk_fp8_f32(a, b, 0, false); w = __builtin_amdgcn_cvt_pk_fp8_f32(c, d, w, true); return (unsigned)w; }
;     static __device__ __forceinline__ f32x2 act2(f32x2 g, f32x2 u) {
;         g.x = __builtin_amdgcn_fmed3f(g.x, -24.0f, 7.0f); g.y = __builtin_amdgcn_fmed3f(g.y, -24.0f, 7.0f);
;         u.x = __builtin_amdgcn_fmed3f(u.x, -7.0f, 7.0f); u.y = __builtin_amdgcn_fmed3f(u.y, -7.0f, 7.0f);
;         f32x2 z = g * (-1.702f * 1.4426950408889634f);
;         f32x2 d; d.x = __builtin_amdgcn_exp2f(z.x); d.y = __builtin_amdgcn_exp2f(z.y);
;         d = d + 1.0f;
;         const float r = __builtin_amdgcn_rcpf(d.x * d.y);
;         f32x2 sg; sg.x = r * d.y; sg.y = r * d.x;
;         return (u + 1.0f) * (g * sg);
;     }
;     __device__ __forceinline__ void operator()(const f32x4 (&acc)[2][2][4][2], const pg8::Unit& u, int wr, int wc, int fr, int fq) const {
;         const int e = u.aux;
;         unsigned char* Ht = ws + WS_H2 + (size_t)u.pm * TSF8;
;         const int hc = u.pn * 128 + wc * 32 + 8 * fq;
;         const f32x4 bg0 = *(const f32x4*)(bgate + e * FF + hc), bg1 = *(const f32x4*)(bgate + e * FF + hc + 4);
;         const f32x4 bu0 = *(const f32x4*)(bup + e * FF + hc), bu1 = *(const f32x4*)(bup + e * FF + hc + 4);
; #pragma unroll
;         for (int ai = 0; ai < 2; ++ai)
; #pragma unroll
;             for (int m = 0; m < 4; ++m) { const int rl = ai * 128 + wr * 64 + m * 16 + fr;
;                 const f32x4 g0 = acc[ai][0][m][0] * (1.0f / 64.0f) + bg0, g1 = acc[ai][0][m][1] * (1.0f / 64.0f) + bg1, u0 = acc[ai][1][m][0] * (1.0f / 64.0f) + bu0, u1 = acc[ai][1][m][1] * (1.0f / 64.0f) + bu1;
;                 const f32x2 h0 = act2((f32x2){g0[0], g0[1]}, (f32x2){u0[0], u0[1]}), h1 = act2((f32x2){g0[2], g0[3]}, (f32x2){u0[2], u0[3]});
;                 const f32x2 h2 = act2((f32x2){g1[0], g1[1]}, (f32x2){u1[0], u1[1]}), h3 = act2((f32x2){g1[2], g1[3]}, (f32x2){u1[2], u1[3]});
;                 *(u32x2*)(Ht + (size_t)rl * FF + hc) = (u32x2){pk4_fp8(h0.x, h0.y, h1.x, h1.y), pk4_fp8(h2.x, h2.y, h3.x, h3.y)}; }
	v_add_f32_e32 v35, 1.0, v35
	v_fma_f32 v40, v94, s16, v214
	v_fma_f32 v41, v95, s16, v215
	v_add_f32_e32 v32, 1.0, v32
	v_add_f32_e32 v33, 1.0, v33
	v_mul_f32_e32 v38, v34, v35
	v_med3_f32 v28, v28, s48, v208
	v_med3_f32 v29, v29, s48, v208
	v_mul_f32_e32 v24, v32, v24
	v_mul_f32_e32 v25, v33, v25
	v_med3_f32 v32, v40, s49, v208
	v_med3_f32 v33, v41, s49, v208
	v_rcp_f32_e32 v38, v38
	v_mul_f32_e32 v40, s18, v28
	v_mul_f32_e32 v41, s18, v29
	v_fma_f32 v36, v96, s16, v216
	v_fma_f32 v37, v97, s16, v217
	v_exp_f32_e32 v40, v40
	v_exp_f32_e32 v41, v41
	v_mul_f32_e32 v232, v35, v38
	v_mul_f32_e32 v35, v34, v38
	v_mov_b32_e32 v34, v232
	v_mul_f32_e32 v30, v30, v34
	v_mul_f32_e32 v31, v31, v35
	v_add_f32_e32 v32, 1.0, v32
	v_add_f32_e32 v33, 1.0, v33
	v_add_f32_e32 v34, 1.0, v40
	v_add_f32_e32 v35, 1.0, v41
	v_mul_f32_e32 v30, v32, v30
	v_mul_f32_e32 v31, v33, v31
	v_mul_f32_e32 v38, v34, v35
	v_rcp_f32_e32 v38, v38
	v_med3_f32 v32, v36, s49, v208
	v_med3_f32 v33, v37, s49, v208
	v_mov_b32_e32 v36, v198
	v_mov_b32_e32 v37, v198
	v_cvt_pk_fp8_f32 v36, v26, v27
	v_cvt_pk_fp8_f32 v37, v30, v31
	v_mul_f32_e32 v232, v35, v38
	v_mul_f32_e32 v35, v34, v38
	v_mov_b32_e32 v34, v232
	v_add_f32_e32 v32, 1.0, v32
	v_add_f32_e32 v33, 1.0, v33
	v_mul_f32_e32 v26, v28, v34
	v_mul_f32_e32 v27, v29, v35
	v_cvt_pk_fp8_f32 v36, v24, v25 op_sel:[0,0,1]
	v_mul_f32_e32 v26, v32, v26
	v_mul_f32_e32 v27, v33, v27
	v_add_co_u32_e32 v24, vcc, s60, v22
	v_cvt_pk_fp8_f32 v37, v26, v27 op_sel:[0,0,1]
	v_fma_f32 v14, v74, s16, v222
	v_fma_f32 v15, v75, s16, v223
	v_addc_co_u32_e32 v25, vcc, 0, v23, vcc
	v_med3_f32 v14, v14, s48, v208
	v_med3_f32 v15, v15, s48, v208
	global_store_dwordx2 v[24:25], v[36:37], off
	v_mul_f32_e32 v24, s18, v14
	v_mul_f32_e32 v25, s18, v15
	v_fma_f32 v16, v76, s16, v224
	v_fma_f32 v17, v77, s16, v225
	v_exp_f32_e32 v24, v24
	v_exp_f32_e32 v25, v25
	v_med3_f32 v16, v16, s48, v208
	v_med3_f32 v17, v17, s48, v208
	v_mul_f32_e32 v28, s18, v16
	v_mul_f32_e32 v29, s18, v17
	v_add_f32_e32 v24, 1.0, v24
	v_add_f32_e32 v25, 1.0, v25
	v_exp_f32_e32 v28, v28
	v_mul_f32_e32 v26, v24, v25
	v_rcp_f32_e32 v26, v26
	v_exp_f32_e32 v29, v29
	v_fma_f32 v18, v82, s16, v226
	v_fma_f32 v19, v83, s16, v227
	v_fma_f32 v10, v70, s16, v218
	v_fma_f32 v11, v71, s16, v219
	v_mul_f32_e32 v232, v25, v26
	v_mul_f32_e32 v25, v24, v26
	v_mov_b32_e32 v24, v232
	v_mul_f32_e32 v14, v14, v24
	v_mul_f32_e32 v15, v15, v25
	v_add_f32_e32 v24, 1.0, v28
	v_add_f32_e32 v25, 1.0, v29
	v_med3_f32 v18, v18, s49, v208
	v_mul_f32_e32 v26, v24, v25
	v_rcp_f32_e32 v26, v26
	v_med3_f32 v19, v19, s49, v208
	v_fma_f32 v20, v84, s16, v228
	v_fma_f32 v21, v85, s16, v229
	v_add_f32_e32 v18, 1.0, v18
	v_add_f32_e32 v19, 1.0, v19
	v_med3_f32 v10, v10, s48, v208
	v_mul_f32_e32 v14, v18, v14
	v_mul_f32_e32 v15, v19, v15
	v_med3_f32 v18, v20, s49, v208
	v_med3_f32 v19, v21, s49, v208
	v_mul_f32_e32 v20, v25, v26
	v_mul_f32_e32 v21, v24, v26
	v_med3_f32 v11, v11, s48, v208
	v_mul_f32_e32 v16, v16, v20
	v_mul_f32_e32 v17, v17, v21
	v_mul_f32_e32 v20, s18, v10
	v_mul_f32_e32 v21, s18, v11
	v_add_f32_e32 v18, 1.0, v18
	v_add_f32_e32 v19, 1.0, v19
	v_exp_f32_e32 v20, v20
	v_exp_f32_e32 v21, v21
	v_fma_f32 v12, v72, s16, v220
	v_fma_f32 v13, v73, s16, v221
	v_mul_f32_e32 v16, v18, v16
	v_mul_f32_e32 v17, v19, v17
	v_med3_f32 v12, v12, s48, v208
	v_add_f32_e32 v18, 1.0, v20
	v_add_f32_e32 v19, 1.0, v21
	v_med3_f32 v13, v13, s48, v208
	v_mul_f32_e32 v20, v18, v19
	v_rcp_f32_e32 v20, v20
	v_mul_f32_e32 v24, s18, v12
	v_mul_f32_e32 v25, s18, v13
	v_fma_f32 v6, v78, s16, v214
	v_fma_f32 v7, v79, s16, v215
	v_exp_f32_e32 v24, v24
	v_exp_f32_e32 v25, v25
	v_mul_f32_e32 v232, v19, v20
	v_mul_f32_e32 v19, v18, v20
	v_mov_b32_e32 v18, v232
	v_mul_f32_e32 v10, v10, v18
	v_mul_f32_e32 v11, v11, v19
	v_med3_f32 v6, v6, s49, v208
	v_add_f32_e32 v18, 1.0, v24
	v_add_f32_e32 v19, 1.0, v25
	v_med3_f32 v7, v7, s49, v208
	v_mul_f32_e32 v20, v18, v19
	v_rcp_f32_e32 v20, v20
	v_add_f32_e32 v6, 1.0, v6
	v_add_f32_e32 v7, 1.0, v7
	v_fma_f32 v8, v80, s16, v216
	v_fma_f32 v9, v81, s16, v217
	v_mul_f32_e32 v6, v6, v10
	v_mul_f32_e32 v7, v7, v11
	v_mul_f32_e32 v10, v19, v20
	v_mul_f32_e32 v11, v18, v20
	v_mov_b32_e32 v18, v198
	v_mov_b32_e32 v19, v198
	v_cvt_pk_fp8_f32 v18, v14, v15
	v_cvt_pk_fp8_f32 v19, v6, v7
	v_med3_f32 v8, v8, s49, v208
	v_med3_f32 v9, v9, s49, v208
	v_add_f32_e32 v8, 1.0, v8
	v_add_f32_e32 v9, 1.0, v9
	v_mul_f32_e32 v6, v12, v10
	v_mul_f32_e32 v7, v13, v11
	v_cvt_pk_fp8_f32 v18, v16, v17 op_sel:[0,0,1]
	v_mul_f32_e32 v6, v8, v6
	v_mul_f32_e32 v7, v9, v7
	s_nop 0
	v_cvt_pk_fp8_f32 v19, v6, v7 op_sel:[0,0,1]
	v_add_co_u32_e32 v6, vcc, 0x2c000, v22
	s_nop 1
	v_addc_co_u32_e32 v7, vcc, 0, v23, vcc
	s_and_b64 vcc, exec, s[2:3]
	s_mov_b64 s[2:3], -1
	global_store_dwordx2 v[6:7], v[18:19], off
	s_cbranch_vccnz .LBB0_956
	s_andn2_b64 vcc, exec, s[10:11]
	s_mov_b64 s[22:23], s[8:9]
	s_mov_b64 s[24:25], s[20:21]
	s_cbranch_vccnz .LBB0_972
	s_lshl_b32 s2, s41, 3
	s_add_i32 s2, s2, s39
	s_ashr_i32 s3, s2, 31
	s_lshl_b64 s[2:3], s[2:3], 18
	s_add_u32 s22, s37, s2
	s_addc_u32 s23, s38, s3
	s_mov_b64 s[24:25], s[6:7]
